# attention loop: waves 0-3 stream K/V tiles, waves 4-7 convert w_up experts 0-15 in-loop via LDS-DMA staging (dedicated conversion halved); on top of v25
# speedup vs baseline: 1.0074x; 1.0074x over previous
; #define LAS __attribute__((address_space(3)))
; __device__ __forceinline__ int fresh_lane() { int l; asm volatile("v_mbcnt_lo_u32_b32 %0, -1, 0\n\tv_mbcnt_hi_u32_b32 %0, -1, %0" : "=v"(l)); return l; }
; __device__ __forceinline__ KP kargs() { KP kp = (KP)__builtin_amdgcn_kernarg_segment_ptr(); asm volatile("" : "+s"(kp)); return kp; }
; __device__ __forceinline__ void conv_run(KP kp, unsigned char* ws, LAS unsigned* P, int lane, int first, int it_hi, int step) {
;     if (first >= it_hi) return;
;     const int lastv = first + ((it_hi - 1 - first) / step) * step;
;     f32x4 a0[8], b0[8], a1[8], b1[8];
;     ConvSrc c0 = conv_decode(kp, ws, first), c1;
; __device__ __forceinline__ void phase3(KP kp, char* lds, LAS unsigned char* ldsl, int wave, int bid, int G) {
;     ...
;             if (pass == 0) { conv_run(kargs(), KWS(), (LAS unsigned*)(ldsl + wave * 8320), fresh_lane(), CONV_DENSE_ITEMS + bid * NWAVES + wave, CONV_UP_END, G * NWAVES); __syncthreads(); }
.LBB0_316:
	s_cmp_lt_i32 s84, 4
	s_cselect_b64 s[2:3], -1, 0
	s_cmp_gt_i32 s85, 3
	s_cselect_b64 s[4:5], -1, 0
	s_and_b64 s[2:3], s[2:3], s[4:5]
	s_andn2_b64 vcc, exec, s[2:3]
	s_cbranch_vccnz .LBB0_706
	s_cmpk_gt_i32 s81, 0xff
	v_writelane_b32 v246, s66, 0
	v_writelane_b32 v246, s92, 1
	s_mov_b64 s[2:3], s[0:1]
	s_waitcnt vmcnt(0)
	v_mbcnt_lo_u32_b32 v0, -1, 0
	v_mbcnt_hi_u32_b32 v0, -1, v0
	v_writelane_b32 v246, s93, 2
	v_writelane_b32 v246, s90, 3
	v_writelane_b32 v246, s83, 4
	v_writelane_b32 v246, s88, 5
	s_nop 1
	v_writelane_b32 v246, s89, 6
	v_writelane_b32 v246, s86, 7
	s_nop 1
	v_writelane_b32 v246, s87, 8
	v_writelane_b32 v246, s82, 9
	v_writelane_b32 v246, s81, 10
	s_cbranch_scc1 .LBB0_656
	v_readlane_b32 s5, v246, 9
	s_mul_i32 s4, s5, 0x2080
	v_readlane_b32 s92, v246, 10
	s_add_i32 s68, s4, 0
	s_lshl_b32 s4, s92, 3
	s_add_i32 s72, s5, s4
	s_add_i32 s18, s72, 0xac00
	s_lshl_b32 s70, s16, 3
	s_cmp_lt_i32 s18, 0x12c00
	s_cselect_b64 s[8:9], -1, 0
	s_sub_i32 s4, 0x7fff, s72
	v_mov_b32_e32 v0, 0x2400
	s_cmpk_gt_i32 s18, 0x1fff
	v_sub_co_u32_e32 v0, vcc, s18, v0
	v_mov_b32_e32 v1, 0x2800
	s_cselect_b64 s[10:11], -1, 0
	s_xor_b64 s[12:13], vcc, -1
	v_sub_co_u32_e32 v1, vcc, s18, v1
	s_load_dwordx2 s[28:29], s[2:3], 0xc8
	s_xor_b64 s[14:15], vcc, -1
	s_cmpk_gt_u32 s18, 0x2bff
	s_mov_b32 s7, 0
	s_waitcnt lgkmcnt(0)
	s_cselect_b64 s[26:27], -1, 0
	s_mov_b32 s6, 16
	s_lshl_b64 s[30:31], s[6:7], 25
	s_and_b32 s71, s72, 0x7ff
	s_addk_i32 s72, 0xc00
	s_lshl_b32 s73, s16, 4
	s_add_u32 s74, s28, 0x38000000
	s_addc_u32 s75, s29, 0
	s_add_u32 s76, s28, 0x3a000000
	s_addc_u32 s77, s29, 0
	s_add_u32 s78, s28, 0x3c000000
	s_addc_u32 s79, s29, 0
	s_add_u32 s80, s28, 0x48000000
	s_addc_u32 s81, s29, 0
	s_lshl_b64 s[2:3], s[6:7], 24
	s_add_u32 s82, s28, 0x6000000
	s_addc_u32 s83, s29, 0
	s_add_u32 s34, s82, s2
	s_addc_u32 s35, s83, s3
	s_add_u32 s36, s28, 0x5800000
	s_addc_u32 s37, s29, 0
	s_add_u32 s38, s28, 0x4800000
	s_addc_u32 s39, s29, 0
	s_add_u32 s40, s28, 0x800000
	s_addc_u32 s41, s29, 0
	s_add_u32 s84, s28, 0x26000000
	s_addc_u32 s85, s29, 0
	s_abs_i32 s2, s70
	v_cvt_f32_u32_e32 v2, s2
	v_readfirstlane_b32 s86, v0
	s_sub_i32 s6, 0, s2
	s_abs_i32 s5, s4
	v_rcp_iflag_f32_e32 v2, v2
	s_ashr_i32 s3, s4, 31
	v_readfirstlane_b32 s87, v1
	v_mov_b32_e32 v1, 0
	v_mul_f32_e32 v0, 0x4f7ffffe, v2
	v_cvt_u32_f32_e32 v0, v0
	s_mov_b64 s[42:43], 0x3c004000
	s_mov_b64 s[44:45], 0x3c204000
	s_brev_b32 s91, 1
	v_readfirstlane_b32 s17, v0
	s_mul_i32 s6, s6, s17
	s_mul_hi_u32 s6, s17, s6
	s_add_i32 s17, s17, s6
	s_mul_hi_u32 s6, s5, s17
	s_mul_i32 s6, s6, s2
	s_sub_i32 s5, s5, s6
	s_sub_i32 s6, s5, s2
	s_cmp_ge_u32 s5, s2
	s_cselect_b32 s5, s6, s5
	s_sub_i32 s6, s5, s2
	s_cmp_ge_u32 s5, s2
	s_cselect_b32 s2, s6, s5
	s_xor_b32 s2, s2, s3
	s_sub_i32 s2, s3, s2
	s_add_i32 s88, s4, s2
	v_mbcnt_lo_u32_b32 v0, -1, 0
	s_add_i32 s88, s88, s18
	s_lshl_b32 s89, s92, 1
	s_lshl_b32 s90, s16, 1
	v_mbcnt_hi_u32_b32 v194, -1, v0
	v_mov_b32_e32 v195, 0xff800000
	s_branch .LBB0_320

; __device__ __forceinline__ int v_rd_base(int lane) { return ((lane & 3) << 3) | (((lane >> 2) & 3) << 6) | (((lane >> 4) & 1) << 5) | (((lane >> 5) & 1) << 8); }
; #define A3_LAS __attribute__((address_space(3)))
; __device__ __forceinline__ void block(const Blk& B, char* lds, A3_LAS unsigned char* ldsl, const int tid) {
;     const int wid = __builtin_amdgcn_readfirstlane(tid >> 6), lane = tid & 63, r32 = lane & 31, hi = lane >> 5;
;     const int NT = (B.P0 + QB3) / 64;
;     char* K_lds = lds + KOFF; char* V_lds = lds + VOFF;
;     float* sc_l = (float*)(lds + SCOFF) + wid * 64;
;     const int vb0 = (int)(uintptr_t)V_lds + attn::v_rd_base(lane);
;     const int qlo = B.P0 + wid * 32, qm = qlo + r32 - 4 * hi;
;     constexpr float C2 = 1.4426950408889634f * attn::SCALE;
;     unsigned kso[2], vso[2];
; #pragma unroll
;     for (int i = 0; i < 2; ++i) { const int row = (2 * wid + i) * 4 + (lane >> 4); const int c = (lane & 15) ^ (row & 7); kso[i] = (unsigned)(row * 128 + c * 8) * 2u; }
; #pragma unroll
;     for (int q = 0; q < 2; ++q) { const int st = 2 * (2 * wid + q) + (lane >> 5), w16 = lane & 31; const int k = (st >> 2) * 8 + (w16 >> 2);
;         const int c = (st & 3) * 32 + (w16 & 3) * 8; vso[q] = (unsigned)(k * 128 + c) * 2u; }
;     ...
;     float m_reg = -1e30f, l_reg = 0.f; bf16x8 qr[8]; f32x16 o[8] = {};
; #pragma unroll
;     for (int d0 = 0; d0 < 8; ++d0) qr[d0] = attn::load8<abf>(B.Q + (size_t)(wid * 32 + r32) * 128 + d0 * 16 + hi * 8);
;     A3_STAGE(0, 0);
;     asm volatile("s_waitcnt vmcnt(0)" ::: "memory");
;     __syncthreads();
.LBB0_323:
	s_cmp_eq_u32 s4, s94
	s_cselect_b32 s6, s95, s93
	s_lshl_b32 s17, s6, 8
	s_lshl_b32 s2, s6, 16
	v_mbcnt_lo_u32_b32 v197, -1, 0
	v_mbcnt_hi_u32_b32 v197, -1, v197
	s_add_u32 s2, s96, s2
	v_add_u32_e32 v0, s33, v197
	s_addc_u32 s3, s97, 0
	v_readfirstlane_b32 s4, v0
	s_ashr_i32 s5, s4, 6
	v_bfe_u32 v0, v197, 4, 2
	s_waitcnt vmcnt(23)
	v_lshl_or_b32 v2, s5, 3, v0
	v_bitop3_b32 v0, v0, v197, 15 bitop3:0x78
	v_lshlrev_b32_e32 v0, 4, v0
	v_and_b32_e32 v3, 15, v197
	v_lshl_or_b32 v199, v2, 8, v0
	v_or_b32_e32 v0, 4, v2
	v_bitop3_b32 v2, v0, v3, 7 bitop3:0x6c
	v_lshlrev_b32_e32 v0, 8, v0
	s_waitcnt vmcnt(21)
	v_lshlrev_b32_e32 v6, 3, v197
	v_lshl_or_b32 v200, v2, 4, v0
	v_and_b32_e32 v0, 24, v6
	v_lshlrev_b32_e32 v2, 5, v197
	v_and_b32_e32 v196, 31, v197
	s_lshl_b32 s56, s5, 5
	v_and_or_b32 v0, v197, 32, v0
	s_lshl_b32 s19, s5, 10
	v_and_b32_e32 v2, 0x380, v2
	v_or3_b32 v0, s19, v2, v0
	v_or_b32_e32 v2, s56, v196
	v_ashrrev_i32_e32 v3, 31, v2
	v_bfe_u32 v198, v197, 5, 1
	v_lshlrev_b64 v[4:5], 8, v[2:3]
	v_lshlrev_b32_e32 v201, 1, v0
	v_lshl_add_u64 v[4:5], s[2:3], 0, v[4:5]
	v_lshlrev_b32_e32 v0, 4, v198
	v_lshl_add_u64 v[4:5], v[4:5], 0, v[0:1]
	s_lshl_b32 s2, s5, 11
	v_or_b32_e32 v202, 0x80, v201
	global_load_dwordx4 v[162:165], v[4:5], off
	global_load_dwordx4 v[166:169], v[4:5], off offset:32
	global_load_dwordx4 v[170:173], v[4:5], off offset:64
	global_load_dwordx4 v[174:177], v[4:5], off offset:96
	global_load_dwordx4 v[178:181], v[4:5], off offset:128
	global_load_dwordx4 v[182:185], v[4:5], off offset:160
	global_load_dwordx4 v[186:189], v[4:5], off offset:192
	global_load_dwordx4 v[190:193], v[4:5], off offset:224
	s_add_i32 s19, s2, 0
	v_mov_b32_e32 v3, v201
	v_mov_b32_e32 v4, v200
	v_mov_b32_e32 v5, v202
	v_mov_b32_e32 v7, v199
	s_mov_b32 m0, s19
	s_and_b32 s3, s4, 0x3fffffc0
	global_load_lds_dwordx4 v7, s[46:47]
	s_add_i32 m0, s19, 0x400
	s_lshl_b32 s3, s3, 2
	global_load_lds_dwordx4 v4, s[46:47]
	s_add_i32 m0, s19, 0x8000
	s_add_i32 s2, s17, 0x100
	global_load_lds_dwordx4 v3, s[48:49]
	s_add_i32 m0, s19, 0xc000
	s_add_i32 s3, s3, 0
	global_load_lds_dwordx4 v3, s[50:51]
	s_add_i32 m0, s19, 0x8400
	s_add_i32 s4, s3, 0x18000
	global_load_lds_dwordx4 v5, s[48:49]
	s_add_i32 m0, s19, 0xc400
	s_add_i32 s23, s56, s17
	global_load_lds_dwordx4 v5, s[50:51]
	s_lshr_b32 s57, s2, 6
	v_lshlrev_b32_e32 v5, 4, v197
	v_lshlrev_b32_e32 v8, 1, v197
	s_movk_i32 s2, 0x70
	v_and_b32_e32 v8, 32, v8
	v_and_b32_e32 v9, 0x70, v5
	v_bitop3_b32 v206, v0, v5, s2 bitop3:0x78
	s_movk_i32 s2, 0x60
	v_lshl_add_u32 v204, v196, 2, s4
	v_add_u32_e32 v203, s4, v0
	s_movk_i32 s4, 0x118
	s_cmp_lg_u32 0, -1
	v_bitop3_b32 v207, v0, v9, 32 bitop3:0x36
	v_bitop3_b32 v208, v0, v9, 64 bitop3:0x36
	v_bitop3_b32 v209, v0, v9, s2 bitop3:0x36
	v_and_or_b32 v0, v6, s4, v8
	s_cselect_b32 s4, 0, 0
	v_and_b32_e32 v3, 63, v197
	v_lshlrev_b32_e32 v4, 2, v198
	v_and_b32_e32 v7, 0xc0, v5
	s_add_i32 s4, s4, 0x8000
	s_waitcnt vmcnt(0)
	v_mov_b32_e32 v14, v1
	v_mov_b32_e32 v15, v1
	s_waitcnt vmcnt(0)
	v_cmp_gt_u32_e64 s[2:3], 32, v3
	v_add3_u32 v210, v7, s4, v0
	v_sub_u32_e32 v211, v2, v4
	v_mov_b32_e32 v0, v1
	v_mov_b32_e32 v2, v1
	v_mov_b32_e32 v3, v1
	v_mov_b32_e32 v4, v1
	v_mov_b32_e32 v5, v1
	v_mov_b32_e32 v6, v1
	v_mov_b32_e32 v7, v1
	v_mov_b32_e32 v8, v1
	v_mov_b32_e32 v9, v1
	v_mov_b32_e32 v10, v1
	v_mov_b32_e32 v11, v1
	v_mov_b32_e32 v12, v1
	v_mov_b32_e32 v13, v1
	v_mov_b64_e32 v[128:129], v[14:15]
	v_mov_b64_e32 v[112:113], v[14:15]
	v_mov_b64_e32 v[96:97], v[14:15]
	v_mov_b64_e32 v[80:81], v[14:15]
	v_mov_b64_e32 v[64:65], v[14:15]
	v_mov_b64_e32 v[48:49], v[14:15]
	v_mov_b64_e32 v[32:33], v[14:15]
	v_mov_b64_e32 v[126:127], v[12:13]
	v_mov_b64_e32 v[124:125], v[10:11]
	v_mov_b64_e32 v[122:123], v[8:9]
	v_mov_b64_e32 v[120:121], v[6:7]
	v_mov_b64_e32 v[118:119], v[4:5]
	v_mov_b64_e32 v[116:117], v[2:3]
	v_mov_b64_e32 v[114:115], v[0:1]
	v_mov_b64_e32 v[110:111], v[12:13]
	v_mov_b64_e32 v[108:109], v[10:11]
	v_mov_b64_e32 v[106:107], v[8:9]
	v_mov_b64_e32 v[104:105], v[6:7]
	v_mov_b64_e32 v[102:103], v[4:5]
	v_mov_b64_e32 v[100:101], v[2:3]
	v_mov_b64_e32 v[98:99], v[0:1]
	v_mov_b64_e32 v[94:95], v[12:13]
	v_mov_b64_e32 v[92:93], v[10:11]
	v_mov_b64_e32 v[90:91], v[8:9]
	v_mov_b64_e32 v[88:89], v[6:7]
	v_mov_b64_e32 v[86:87], v[4:5]
	v_mov_b64_e32 v[84:85], v[2:3]
	v_mov_b64_e32 v[82:83], v[0:1]
	v_mov_b64_e32 v[78:79], v[12:13]
	v_mov_b64_e32 v[76:77], v[10:11]
	v_mov_b64_e32 v[74:75], v[8:9]
	v_mov_b64_e32 v[72:73], v[6:7]
	v_mov_b64_e32 v[70:71], v[4:5]
	v_mov_b64_e32 v[68:69], v[2:3]
	v_mov_b64_e32 v[66:67], v[0:1]
	v_mov_b64_e32 v[62:63], v[12:13]
	v_mov_b64_e32 v[60:61], v[10:11]
	v_mov_b64_e32 v[58:59], v[8:9]
	v_mov_b64_e32 v[56:57], v[6:7]
	v_mov_b64_e32 v[54:55], v[4:5]
	v_mov_b64_e32 v[52:53], v[2:3]
	v_mov_b64_e32 v[50:51], v[0:1]
	v_mov_b64_e32 v[46:47], v[12:13]
	v_mov_b64_e32 v[44:45], v[10:11]
	v_mov_b64_e32 v[42:43], v[8:9]
	v_mov_b64_e32 v[40:41], v[6:7]
	v_mov_b64_e32 v[38:39], v[4:5]
	v_mov_b64_e32 v[36:37], v[2:3]
	v_mov_b64_e32 v[34:35], v[0:1]
	v_mov_b64_e32 v[30:31], v[12:13]
	v_mov_b64_e32 v[28:29], v[10:11]
	v_mov_b64_e32 v[26:27], v[8:9]
	v_mov_b64_e32 v[24:25], v[6:7]
	v_mov_b64_e32 v[22:23], v[4:5]
	v_mov_b64_e32 v[20:21], v[2:3]
	v_mov_b64_e32 v[18:19], v[0:1]
	v_mov_b64_e32 v[16:17], v[14:15]
	s_mov_b32 s5, 1
	v_lshlrev_b32_e32 v205, 8, v196
	v_mov_b32_e32 v212, 0
	v_mov_b32_e32 v213, 0xf149f2ca
	s_movk_i32 s62, 0xff00
	s_mov_b64 s[58:59], s[28:29]
	v_mov_b64_e32 v[14:15], v[12:13]
	v_mov_b64_e32 v[12:13], v[10:11]
	v_mov_b64_e32 v[10:11], v[8:9]
	v_mov_b64_e32 v[8:9], v[6:7]
	v_mov_b64_e32 v[6:7], v[4:5]
	v_mov_b64_e32 v[4:5], v[2:3]
	v_mov_b64_e32 v[2:3], v[0:1]
	s_load_dwordx2 s[98:99], s[0:1], 0x98
	s_waitcnt vmcnt(0) lgkmcnt(0)
	s_barrier
; __device__ __forceinline__ void block(const Blk& B, char* lds, A3_LAS unsigned char* ldsl, const int tid) {
;     ...
;     for (int i = 0; i < 2; ++i) { const int row = (2 * wid + i) * 4 + (lane >> 4); const int c = (lane & 15) ^ (row & 7); kso[i] = (unsigned)(row * 128 + c * 8) * 2u; }
; #pragma unroll
;     for (int q = 0; q < 2; ++q) { const int st = 2 * (2 * wid + q) + (lane >> 5), w16 = lane & 31; const int k = (st >> 2) * 8 + (w16 >> 2);
;         const int c = (st & 3) * 32 + (w16 & 3) * 8; vso[q] = (unsigned)(k * 128 + c) * 2u; }
;     ...
;     float m_reg = -1e30f, l_reg = 0.f; bf16x8 qr[8]; f32x16 o[8] = {};
; #pragma unroll
;     for (int d0 = 0; d0 < 8; ++d0) qr[d0] = attn::load8<abf>(B.Q + (size_t)(wid * 32 + r32) * 128 + d0 * 16 + hi * 8);
;     A3_STAGE(0, 0);
;     asm volatile("s_waitcnt vmcnt(0)" ::: "memory");
;     __syncthreads();
;     for (int t = 0; t < NT; ++t) {
;         const int buf = t & 1, kb = t * 64;
;         if (t + 1 < NT) A3_STAGE(t + 1, buf ^ 1);
;         f32x16 p0, p1;
;         attn::qkt<0, false>(p0, p1, K_lds + buf * 16384, r32, hi, qr, true);
	s_lshr_b32 s64, s92, 3
	s_lshl_b32 s64, s64, 20
	s_and_b32 s65, s92, 7
	s_lshl_b32 s65, s65, 11
	s_add_u32 s64, s64, s65
	s_add_u32 s98, s98, s64
	s_addc_u32 s99, s99, 0
	s_lshr_b32 s64, s92, 3
	s_lshl_b32 s64, s64, 15
	s_and_b32 s65, s92, 7
	s_lshl_b32 s65, s65, 21
	s_add_u32 s64, s64, s65
	s_add_u32 s64, s64, 0x6000000
	s_add_u32 s100, s28, s64
	s_addc_u32 s101, s29, 0
	s_sub_i32 s32, 0x82, s57
	s_cmp_eq_u64 s[54:55], 0
	s_cselect_b32 s32, s32, 0
	s_mov_b32 s63, 0
	s_lshr_b32 s64, s19, 11
	s_sub_i32 s64, s64, 4
	s_lshl_b32 s64, s64, 1
	s_or_b32 s65, s64, 1
	v_lshrrev_b32_e32 v214, 4, v197
	v_lshl_add_u32 v214, s64, 3, v214
	v_lshlrev_b32_e32 v214, 14, v214
	v_and_b32_e32 v215, 15, v197
	v_xor_b32_e32 v215, s64, v215
	v_lshl_add_u32 v247, v215, 4, v214
	v_and_b32_e32 v214, 7, v197
	v_lshrrev_b32_e32 v215, 5, v197
	v_lshl_add_u32 v215, s64, 1, v215
	v_xor_b32_e32 v215, v215, v214
	v_lshlrev_b32_e32 v215, 4, v215
	v_lshl_add_u32 v215, v214, 11, v215
	v_bfe_u32 v216, v197, 3, 2
	v_lshl_add_u32 v215, v216, 2, v215
	v_add_u32_e32 v249, 0x19000, v215
	v_lshlrev_b32_e32 v214, 4, v197
	v_lshl_add_u32 v251, s64, 10, v214
	v_lshrrev_b32_e32 v214, 4, v197
	v_lshl_add_u32 v214, s65, 3, v214
	v_lshlrev_b32_e32 v214, 14, v214
	v_and_b32_e32 v215, 15, v197
	v_xor_b32_e32 v215, s65, v215
	v_lshl_add_u32 v248, v215, 4, v214
	v_and_b32_e32 v214, 7, v197
	v_lshrrev_b32_e32 v215, 5, v197
	v_lshl_add_u32 v215, s65, 1, v215
	v_xor_b32_e32 v215, v215, v214
	v_lshlrev_b32_e32 v215, 4, v215
	v_lshl_add_u32 v215, v214, 11, v215
	v_bfe_u32 v216, v197, 3, 2
	v_lshl_add_u32 v215, v216, 2, v215
	v_add_u32_e32 v250, 0x19000, v215
.LBB0_324:
	s_add_i32 s4, s5, -1
	s_and_b32 s20, s4, 1
	s_lshl_b32 s4, s20, 14
	v_add3_u32 v245, s4, v206, v205
	v_add3_u32 v242, s4, v207, v205
	v_add3_u32 v243, s4, v208, v205
	v_add3_u32 v244, s4, v209, v205
	ds_read_b128 v[214:217], v245
	ds_read_b128 v[218:221], v242
	ds_read_b128 v[130:133], v245 offset:8192
	ds_read_b128 v[222:225], v242 offset:8192
	ds_read_b128 v[226:229], v243
	ds_read_b128 v[230:233], v243 offset:8192
	ds_read_b128 v[234:237], v244
	ds_read_b128 v[238:241], v244 offset:8192
	s_cmp_lt_u32 s19, 0x2000
	s_cbranch_scc0 .Latt_conv_issue
	s_cmp_lt_u32 s5, s57
	s_cbranch_scc0 .Latt_x_noload
	s_lshl_b32 s60, s19, 1
	s_xor_b32 s21, s4, 0x4000
	s_add_i32 s21, s60, s21
	s_lshl_b32 s64, s20, 15
	s_xor_b32 s64, s64, 0x8000
	s_add_i32 s64, s60, s64
	s_add_u32 s60, s58, s25
	s_addc_u32 s61, s59, s22
	s_add_u32 s60, s60, s19
	s_addc_u32 s61, s61, 0
	s_mov_b32 m0, s21
	s_nop 0
	global_load_lds_dwordx4 v199, s[60:61]
	s_add_i32 m0, s21, 0x400
	s_nop 0
	global_load_lds_dwordx4 v200, s[60:61]
	s_add_u32 s60, s60, 0x800
	s_addc_u32 s61, s61, 0
	s_add_i32 m0, s21, 0x800
	s_nop 0
	global_load_lds_dwordx4 v199, s[60:61]
	s_add_i32 m0, s21, 0xc00
	s_nop 0
	global_load_lds_dwordx4 v200, s[60:61]
	s_add_u32 s60, s58, s52
	s_addc_u32 s61, s59, s53
	s_add_u32 s60, s60, s19
	s_addc_u32 s61, s61, 0
	v_mov_b32_e32 v0, v201
	v_lshl_add_u64 v[146:147], s[60:61], 0, v[0:1]
	v_lshl_add_u64 v[148:149], v[146:147], 0, s[42:43]
	s_add_i32 m0, s64, 0x8000
	v_lshl_add_u64 v[146:147], v[146:147], 0, s[44:45]
	global_load_lds_dwordx4 v[148:149], off
	s_add_i32 m0, s64, 0xc000
	s_nop 0
	global_load_lds_dwordx4 v[146:147], off
	v_mov_b32_e32 v0, v202
	v_lshl_add_u64 v[146:147], s[60:61], 0, v[0:1]
	v_lshl_add_u64 v[148:149], v[146:147], 0, s[42:43]
	s_add_i32 m0, s64, 0x8400
	v_lshl_add_u64 v[146:147], v[146:147], 0, s[44:45]
	global_load_lds_dwordx4 v[148:149], off
	s_add_i32 m0, s64, 0xc400
	s_nop 0
	global_load_lds_dwordx4 v[146:147], off
	s_add_u32 s60, s60, 0x800
	s_addc_u32 s61, s61, 0
	v_mov_b32_e32 v0, v201
	v_lshl_add_u64 v[146:147], s[60:61], 0, v[0:1]
	v_lshl_add_u64 v[148:149], v[146:147], 0, s[42:43]
	s_add_i32 m0, s64, 0x8800
	v_lshl_add_u64 v[146:147], v[146:147], 0, s[44:45]
	global_load_lds_dwordx4 v[148:149], off
	s_add_i32 m0, s64, 0xc800
	s_nop 0
	global_load_lds_dwordx4 v[146:147], off
	v_mov_b32_e32 v0, v202
	v_lshl_add_u64 v[146:147], s[60:61], 0, v[0:1]
	v_lshl_add_u64 v[148:149], v[146:147], 0, s[42:43]
	s_add_i32 m0, s64, 0x8c00
	v_lshl_add_u64 v[146:147], v[146:147], 0, s[44:45]
	global_load_lds_dwordx4 v[148:149], off
	s_add_i32 m0, s64, 0xcc00
	s_nop 0
	global_load_lds_dwordx4 v[146:147], off
	s_branch .Latt_x_noload
; #define GAS __attribute__((address_space(1)))
; #define LAS __attribute__((address_space(3)))
; template <int KB, bool SK>
; __device__ __forceinline__ void qkt(f32x16& p0, f32x16& p1, const char* K_lds, int r32, int hi, const bf16x8* qr, bool act) {
;     ...
;     for (int dd = 0; dd < 4; ++dd) kb[dd] = K_lds + KB * SHM_K + KSWZ(r32, (dd * 16 + hi * 8) * 2);
; #pragma unroll
;     for (int d0 = 0; d0 < 8; ++d0) { const char* a = kb[d0 & 3] + (d0 >> 2) * 128;
;         bf16x8 b0 = *reinterpret_cast<const bf16x8*>(a);
;         bf16x8 b1 = *reinterpret_cast<const bf16x8*>(a + 32 * 256);
;         p0 = __builtin_amdgcn_mfma_f32_32x32x16_bf16(b0, qr[d0], p0, 0, 0, 0);
;         p1 = __builtin_amdgcn_mfma_f32_32x32x16_bf16(b1, qr[d0], p1, 0, 0, 0); }
; __device__ __forceinline__ void conv_emit(const ConvSrc& c, int lane, LAS unsigned* P, const f32x4 (&ra)[8], const f32x4 (&rb)[8]) {
;     ...
;     for (int jj = 0; jj < 8; ++jj) { const int n = (lane >> 3) + 8 * jj; const LAS unsigned* sp = P + (4 * cc) * 65 + n;
;         v4u o; o.x = sp[0]; o.y = sp[65]; o.z = sp[130]; o.w = sp[195];
;         bf16* dst = c.tiled ? c.WT + (size_t)((nb >> 2) * c.tiled + c.ktoff + kb) * 16384 + ((nb & 3) * 64 + n) * 64 + 8 * cc : c.WT + (size_t)(n0 + n) * c.ldk + k0 + 8 * cc;
;         __builtin_nontemporal_store(o, (GAS v4u*)dst); }
.Latt_conv_issue:
	s_lshr_b32 s60, s32, 3
	s_and_b32 s61, s32, 7
	s_lshl_b32 s61, s61, 8
	s_lshl_b32 s21, s60, 25
	s_add_u32 s21, s21, s61
	s_add_u32 s64, s98, s21
	s_addc_u32 s65, s99, 0
	s_sub_i32 s60, s19, 0x2000
	s_lshl_b32 s60, s60, 1
	s_add_i32 s60, s60, s63
	s_add_i32 m0, s60, 0x19000
	s_nop 0
	global_load_lds_dwordx4 v247, s[64:65]
	s_add_i32 m0, s60, 0x19800
	s_nop 0
	global_load_lds_dwordx4 v248, s[64:65]
	s_add_u32 s64, s64, 0x10000
	s_addc_u32 s65, s65, 0
	s_add_i32 m0, s60, 0x19400
	s_nop 0
	global_load_lds_dwordx4 v247, s[64:65]
	s_add_i32 m0, s60, 0x19c00
	s_nop 0
	global_load_lds_dwordx4 v248, s[64:65]
.Latt_x_noload:
	s_add_i32 s32, s32, 1
	s_waitcnt lgkmcnt(7)
	v_mfma_f32_32x32x16_bf16 v[146:161], v[214:217], v[162:165], 0
	ds_read_b128 v[214:217], v245 offset:128
	s_waitcnt lgkmcnt(7)
	v_mfma_f32_32x32x16_bf16 v[146:161], v[218:221], v[166:169], v[146:161]
	ds_read_b128 v[218:221], v245 offset:8320
	s_waitcnt lgkmcnt(7)
	v_mfma_f32_32x32x16_bf16 v[130:145], v[130:133], v[162:165], 0
	s_waitcnt lgkmcnt(6)
	v_mfma_f32_32x32x16_bf16 v[130:145], v[222:225], v[166:169], v[130:145]
	ds_read_b128 v[222:225], v242 offset:128
	s_waitcnt lgkmcnt(6)
	v_mfma_f32_32x32x16_bf16 v[146:161], v[226:229], v[170:173], v[146:161]
	ds_read_b128 v[226:229], v242 offset:8320
	s_waitcnt lgkmcnt(6)
	v_mfma_f32_32x32x16_bf16 v[130:145], v[230:233], v[170:173], v[130:145]
	ds_read_b128 v[230:233], v243 offset:128
	s_waitcnt lgkmcnt(6)
	v_mfma_f32_32x32x16_bf16 v[146:161], v[234:237], v[174:177], v[146:161]
	ds_read_b128 v[234:237], v243 offset:8320
	s_waitcnt lgkmcnt(6)
	v_mfma_f32_32x32x16_bf16 v[130:145], v[238:241], v[174:177], v[130:145]
	ds_read_b128 v[238:241], v244 offset:128
	s_waitcnt lgkmcnt(6)
	v_mfma_f32_32x32x16_bf16 v[146:161], v[214:217], v[178:181], v[146:161]
	ds_read_b128 v[214:217], v244 offset:8320
	s_waitcnt lgkmcnt(6)
	v_mfma_f32_32x32x16_bf16 v[130:145], v[218:221], v[178:181], v[130:145]
	s_waitcnt lgkmcnt(5)
	v_mfma_f32_32x32x16_bf16 v[146:161], v[222:225], v[182:185], v[146:161]
	s_waitcnt lgkmcnt(4)
	v_mfma_f32_32x32x16_bf16 v[130:145], v[226:229], v[182:185], v[130:145]
	s_waitcnt lgkmcnt(3)
	v_mfma_f32_32x32x16_bf16 v[146:161], v[230:233], v[186:189], v[146:161]
	s_waitcnt lgkmcnt(2)
	v_mfma_f32_32x32x16_bf16 v[130:145], v[234:237], v[186:189], v[130:145]
	s_waitcnt lgkmcnt(1)
	v_mfma_f32_32x32x16_bf16 v[146:161], v[238:241], v[190:193], v[146:161]
	s_waitcnt lgkmcnt(0)
	v_mfma_f32_32x32x16_bf16 v[130:145], v[214:217], v[190:193], v[130:145]
	s_cmp_lt_u32 s19, 0x2000
	s_cbranch_scc1 .Latt_nocons1
	s_cmp_lt_u32 s5, 3
	s_cbranch_scc1 .Latt_nocons1
	s_add_i32 s60, s32, -3
	s_lshr_b32 s61, s60, 3
	s_lshl_b32 s61, s61, 24
	s_and_b32 s21, s60, 4
	s_lshl_b32 s21, s21, 18
	s_add_u32 s61, s61, s21
	s_and_b32 s21, s60, 3
	s_lshl_b32 s21, s21, 13
	s_add_u32 s61, s61, s21
	s_add_u32 s64, s100, s61
	s_addc_u32 s65, s101, 0
	s_add_i32 s21, s63, 0x4000
	s_cmp_eq_u32 s21, 0xc000
	s_cselect_b32 s21, 0, s21
	v_add_u32_e32 v238, s21, v249
	v_add_u32_e32 v239, s21, v250
	ds_read_b32 v222, v238
	ds_read_b32 v223, v238 offset:256
	ds_read_b32 v224, v238 offset:512
	ds_read_b32 v225, v238 offset:768
	ds_read_b32 v226, v238 offset:1024
	ds_read_b32 v227, v238 offset:1280
	ds_read_b32 v228, v238 offset:1536
	ds_read_b32 v229, v238 offset:1792
	ds_read_b32 v230, v239
	ds_read_b32 v231, v239 offset:256
	ds_read_b32 v232, v239 offset:512
	ds_read_b32 v233, v239 offset:768
	ds_read_b32 v234, v239 offset:1024
	ds_read_b32 v235, v239 offset:1280
	ds_read_b32 v236, v239 offset:1536
	ds_read_b32 v237, v239 offset:1792

; __device__ __forceinline__ float vmax3(float a, float b, float c) { float d; asm("v_max3_f32 %0, %1, %2, %3" : "=v"(d) : "v"(a), "v"(b), "v"(c)); return d; }
; #define GAS __attribute__((address_space(1)))
; __device__ __forceinline__ void block(const Blk& B, char* lds, A3_LAS unsigned char* ldsl, const int tid) {
;     ...
;         float pmax = fmaxf(p0[15], p1[15]);
;         { float mb;
;           asm("v_max3_f32 %0, %0, %2, %3\n\tv_max3_f32 %1, %10, %11, %12\n\tv_max3_f32 %0, %0, %4, %5\n\tv_max3_f32 %1, %1, %13, %14\n\tv_max3_f32 %0, %0, %6, %7\n\tv_max3_f32 %1, %1, %15, %16\n\tv_max3_f32 %0, %0, %8, %9\n\tv_max3_f32 %1, %1, %17, %18"
;               : "+&v"(pmax), "=&v"(mb) : "v"(p0[0]), "v"(p0[1]), "v"(p0[2]), "v"(p0[3]), "v"(p0[4]), "v"(p0[5]), "v"(p0[6]), "v"(p0[7]),
;                 "v"(p1[0]), "v"(p1[1]), "v"(p1[2]), "v"(p1[3]), "v"(p1[4]), "v"(p1[5]), "v"(p1[6]), "v"(p1[7]), "v"(p1[8]));
;           asm("v_max3_f32 %0, %0, %2, %3\n\tv_max3_f32 %1, %1, %9, %10\n\tv_max3_f32 %0, %0, %4, %5\n\tv_max3_f32 %1, %1, %11, %12\n\tv_max3_f32 %0, %0, %6, %7\n\tv_max3_f32 %1, %1, %13, %14\n\tv_max3_f32 %0, %0, %1, %8"
;               : "+&v"(pmax), "+&v"(mb) : "v"(p0[8]), "v"(p0[9]), "v"(p0[10]), "v"(p0[11]), "v"(p0[12]), "v"(p0[13]), "v"(p0[14]),
;                 "v"(p1[9]), "v"(p1[10]), "v"(p1[11]), "v"(p1[12]), "v"(p1[13]), "v"(p1[14])); }
;         { auto rr = __builtin_amdgcn_permlane32_swap(__float_as_uint(pmax), __float_as_uint(pmax), false, false); pmax = vmax3(__uint_as_float(rr[0]), __uint_as_float(rr[1]), __uint_as_float(rr[1])); }
;         const bool keep = __all((pmax - m_reg) * attn::SCALE <= attn::THR);
;         const float mn = keep ? m_reg : vmax3(m_reg, pmax, pmax); const float alpha = __builtin_amdgcn_exp2f((m_reg - mn) * C2); m_reg = mn;
; __device__ __forceinline__ void conv_emit(const ConvSrc& c, int lane, LAS unsigned* P, const f32x4 (&ra)[8], const f32x4 (&rb)[8]) {
;     ...
;     for (int jj = 0; jj < 8; ++jj) { const int n = (lane >> 3) + 8 * jj; const LAS unsigned* sp = P + (4 * cc) * 65 + n;
;         v4u o; o.x = sp[0]; o.y = sp[65]; o.z = sp[130]; o.w = sp[195];
;         bf16* dst = c.tiled ? c.WT + (size_t)((nb >> 2) * c.tiled + c.ktoff + kb) * 16384 + ((nb & 3) * 64 + n) * 64 + 8 * cc : c.WT + (size_t)(n0 + n) * c.ldk + k0 + 8 * cc;
;         __builtin_nontemporal_store(o, (GAS v4u*)dst); }
.LBB0_330:
	s_nop 10
	s_cmp_lt_u32 s19, 0x2000
	s_cbranch_scc1 .Latt_nocons2
	s_cmp_lt_u32 s5, 3
	s_cbranch_scc1 .Latt_nocons2
	s_waitcnt lgkmcnt(0)
	v_cvt_pk_bf16_f32 v222, v222, v223
	v_cvt_pk_bf16_f32 v223, v224, v225
	v_cvt_pk_bf16_f32 v224, v226, v227
	v_cvt_pk_bf16_f32 v225, v228, v229
	v_cvt_pk_bf16_f32 v230, v230, v231
	v_cvt_pk_bf16_f32 v231, v232, v233
	v_cvt_pk_bf16_f32 v232, v234, v235
	v_cvt_pk_bf16_f32 v233, v236, v237
	global_store_dwordx4 v251, v[222:225], s[64:65]
	global_store_dwordx4 v251, v[230:233], s[64:65] offset:1024
.Latt_nocons2:
	v_max_f32_e32 v0, v145, v145
	v_max_f32_e32 v214, v161, v161
	v_max_f32_e32 v0, v214, v0
	v_max3_f32 v0, v0, v146, v147
	v_max3_f32 v214, v130, v131, v132
	v_max3_f32 v0, v0, v148, v149
	v_max3_f32 v214, v214, v133, v134
	v_max3_f32 v0, v0, v150, v151
	v_max3_f32 v214, v214, v135, v136
	v_max3_f32 v0, v0, v152, v153
	v_max3_f32 v214, v214, v137, v138
	s_mov_b32 s4, 0x41000000
	v_max3_f32 v0, v0, v154, v155
	v_max3_f32 v214, v214, v139, v140
	v_max3_f32 v0, v0, v156, v157
	v_max3_f32 v214, v214, v141, v142
	v_max3_f32 v0, v0, v158, v159
	v_max3_f32 v214, v214, v143, v144
	v_max3_f32 v0, v0, v214, v160
	s_nop 0
	v_mov_b32_e32 v214, v0
	s_nop 1
	v_permlane32_swap_b32_e32 v0, v214
	v_max3_f32 v214, v0, v214, v214
	s_nop 0
	v_sub_f32_e32 v0, v214, v213
	v_mul_f32_e32 v0, 0x3db504f3, v0
	v_cmp_ge_f32_e32 vcc, s4, v0
	s_cmp_eq_u64 vcc, exec
	v_mov_b32_e32 v0, v213
	s_cbranch_scc1 .LBB0_332
	v_max3_f32 v0, v213, v214, v214

; #define A3_RDK(vb, d0, s) do { A3_TRRD(xl##s, vb, (d0) * 512 + (s) * 4096); A3_TRRD(xh##s, vb, (d0) * 512 + (s) * 4096 + 2048); A3_TRRD(yl##s, vb, ((d0) + 1) * 512 + (s) * 4096); A3_TRRD(yh##s, vb, ((d0) + 1) * 512 + (s) * 4096 + 2048); } while (0)
; #define A3_PAIR(accx, accy, NEXT0, NEXT1, NEXT2, NEXT3) do { A3_STEPK(accx, accy, pa0, 0, NEXT0); A3_STEPK(accx, accy, pa1, 1, NEXT1); A3_STEPK(accx, accy, pa2, 2, NEXT2); A3_STEPK(accx, accy, pa3, 3, NEXT3); } while (0)
; #define A3_NONE do { asm volatile("s_waitcnt lgkmcnt(0)" ::: "memory"); } while (0)
; __device__ __forceinline__ float own_sum(const f32x16& P) { return ((P[0] + P[1]) + (P[2] + P[3])) + ((P[4] + P[5]) + (P[6] + P[7])) + (((P[8] + P[9]) + (P[10] + P[11])) + ((P[12] + P[13]) + (P[14] + P[15]))); }
; __device__ __forceinline__ void pv256(f32x16* o, int vb0, bf16x8 pa0, bf16x8 pa1, bf16x8 pa2, bf16x8 pa3) {
;     s16x4 xl0, xh0, xl1, xh1, xl2, xh2, xl3, xh3, yl0, yh0, yl1, yh1, yl2, yh2, yl3, yh3;
;     const int va = vb0, vb = vb0 + 16384;
;     asm volatile("s_waitcnt lgkmcnt(0)" ::: "memory");
;     A3_RDK(va, 0, 0); A3_RDK(va, 0, 1); A3_RDK(va, 0, 2); A3_RDK(va, 0, 3);
;     A3_PAIR(o[0], o[1], A3_RDK(va, 2, 0), A3_RDK(va, 2, 1), A3_RDK(va, 2, 2), A3_RDK(va, 2, 3));
;     A3_PAIR(o[2], o[3], A3_RDK(vb, 0, 0), A3_RDK(vb, 0, 1), A3_RDK(vb, 0, 2), A3_RDK(vb, 0, 3));
;     A3_PAIR(o[4], o[5], A3_RDK(vb, 2, 0), A3_RDK(vb, 2, 1), A3_RDK(vb, 2, 2), A3_RDK(vb, 2, 3));
;     A3_PAIR(o[6], o[7], A3_NONE, A3_NONE, A3_NONE, A3_NONE);
; __device__ __forceinline__ void block(const Blk& B, char* lds, A3_LAS unsigned char* ldsl, const int tid) {
;     ...
;         l_reg = l_reg * alpha + (own_sum(p0) + own_sum(p1));
.LBB0_336:
	v_add_f32_e32 v146, v217, v219
	v_add_f32_e32 v147, v221, v223
	v_add_f32_e32 v146, v146, v147
	v_add_f32_e32 v147, v226, v228
	v_add_f32_e32 v148, v230, v232
	v_add_f32_e32 v147, v147, v148
	v_add_f32_e32 v146, v146, v147
	v_add_f32_e32 v147, v233, v235
	v_add_f32_e32 v148, v238, v240
	v_add_f32_e32 v147, v147, v148
	v_add_f32_e32 v148, v242, v243
	v_add_f32_e32 v149, v244, v245
	v_add_f32_e32 v148, v148, v149
	v_add_f32_e32 v147, v147, v148
	v_add_f32_e32 v146, v146, v147
	v_add_f32_e32 v147, v213, v214
	v_add_f32_e32 v148, v215, v216
	v_add_f32_e32 v147, v147, v148
	v_add_f32_e32 v148, v218, v220
	v_add_f32_e32 v149, v222, v224
	v_add_f32_e32 v148, v148, v149
	v_add_f32_e32 v147, v147, v148
	v_add_f32_e32 v148, v225, v227
	v_add_f32_e32 v149, v229, v231
	v_add_f32_e32 v148, v148, v149
	v_add_f32_e32 v149, v234, v236
	v_add_f32_e32 v150, v239, v241
	v_add_f32_e32 v149, v149, v150
	v_add_f32_e32 v148, v148, v149
	v_add_f32_e32 v147, v147, v148
	s_waitcnt lgkmcnt(0)
	v_add_f32_e32 v146, v147, v146
	v_lshl_add_u32 v147, s20, 15, v210
	ds_read_b64_tr_b16 v[148:149], v147 offset:0
	ds_read_b64_tr_b16 v[150:151], v147 offset:0x800
	ds_read_b64_tr_b16 v[152:153], v147 offset:0x200
	ds_read_b64_tr_b16 v[154:155], v147 offset:0xa00
	ds_read_b64_tr_b16 v[156:157], v147 offset:0x1000
	ds_read_b64_tr_b16 v[158:159], v147 offset:0x1800
	v_fmac_f32_e32 v146, v212, v237
	ds_read_b64_tr_b16 v[212:213], v147 offset:0x1200
	ds_read_b64_tr_b16 v[214:215], v147 offset:0x1a00
	ds_read_b64_tr_b16 v[216:217], v147 offset:0x2000
	ds_read_b64_tr_b16 v[218:219], v147 offset:0x2800
	ds_read_b64_tr_b16 v[220:221], v147 offset:0x2200
	ds_read_b64_tr_b16 v[222:223], v147 offset:0x2a00
	ds_read_b64_tr_b16 v[224:225], v147 offset:0x3000
	ds_read_b64_tr_b16 v[226:227], v147 offset:0x3800
	ds_read_b64_tr_b16 v[228:229], v147 offset:0x3200
	ds_read_b64_tr_b16 v[230:231], v147 offset:0x3a00
	s_waitcnt lgkmcnt(12)
	v_add_u32_e32 v160, 0x4000, v147
	v_mfma_f32_32x32x16_bf16 v[114:129], v[142:145], v[148:151], v[114:129]
	v_mfma_f32_32x32x16_bf16 v[98:113], v[142:145], v[152:155], v[98:113]
	ds_read_b64_tr_b16 v[148:149], v147 offset:0x400
	ds_read_b64_tr_b16 v[150:151], v147 offset:0xc00
	ds_read_b64_tr_b16 v[152:153], v147 offset:0x600
	ds_read_b64_tr_b16 v[154:155], v147 offset:0xe00
	s_waitcnt lgkmcnt(12)
	v_mfma_f32_32x32x16_bf16 v[114:129], v[138:141], v[156:159], v[114:129]
	v_mfma_f32_32x32x16_bf16 v[98:113], v[138:141], v[212:215], v[98:113]
	ds_read_b64_tr_b16 v[156:157], v147 offset:0x1400
	ds_read_b64_tr_b16 v[158:159], v147 offset:0x1c00
	ds_read_b64_tr_b16 v[212:213], v147 offset:0x1600
	ds_read_b64_tr_b16 v[214:215], v147 offset:0x1e00
	s_waitcnt lgkmcnt(12)
	v_mfma_f32_32x32x16_bf16 v[114:129], v[134:137], v[216:219], v[114:129]
	v_mfma_f32_32x32x16_bf16 v[98:113], v[134:137], v[220:223], v[98:113]
	ds_read_b64_tr_b16 v[216:217], v147 offset:0x2400
	ds_read_b64_tr_b16 v[218:219], v147 offset:0x2c00
	ds_read_b64_tr_b16 v[220:221], v147 offset:0x2600
	ds_read_b64_tr_b16 v[222:223], v147 offset:0x2e00
	s_waitcnt lgkmcnt(12)
	v_mfma_f32_32x32x16_bf16 v[114:129], v[130:133], v[224:227], v[114:129]
	v_mfma_f32_32x32x16_bf16 v[98:113], v[130:133], v[228:231], v[98:113]
	ds_read_b64_tr_b16 v[224:225], v147 offset:0x3400
	ds_read_b64_tr_b16 v[226:227], v147 offset:0x3c00
	ds_read_b64_tr_b16 v[228:229], v147 offset:0x3600
	ds_read_b64_tr_b16 v[230:231], v147 offset:0x3e00
	s_waitcnt lgkmcnt(12)
	v_mfma_f32_32x32x16_bf16 v[82:97], v[142:145], v[148:151], v[82:97]
	v_mfma_f32_32x32x16_bf16 v[66:81], v[142:145], v[152:155], v[66:81]
	ds_read_b64_tr_b16 v[148:149], v160 offset:0
	ds_read_b64_tr_b16 v[150:151], v160 offset:0x800
	ds_read_b64_tr_b16 v[152:153], v160 offset:0x200
	ds_read_b64_tr_b16 v[154:155], v160 offset:0xa00
	s_waitcnt lgkmcnt(12)
; #define A3_RDK(vb, d0, s) do { A3_TRRD(xl##s, vb, (d0) * 512 + (s) * 4096); A3_TRRD(xh##s, vb, (d0) * 512 + (s) * 4096 + 2048); A3_TRRD(yl##s, vb, ((d0) + 1) * 512 + (s) * 4096); A3_TRRD(yh##s, vb, ((d0) + 1) * 512 + (s) * 4096 + 2048); } while (0)
; #define A3_PAIR(accx, accy, NEXT0, NEXT1, NEXT2, NEXT3) do { A3_STEPK(accx, accy, pa0, 0, NEXT0); A3_STEPK(accx, accy, pa1, 1, NEXT1); A3_STEPK(accx, accy, pa2, 2, NEXT2); A3_STEPK(accx, accy, pa3, 3, NEXT3); } while (0)
; #define A3_NONE do { asm volatile("s_waitcnt lgkmcnt(0)" ::: "memory"); } while (0)
; __device__ __forceinline__ void pv256(f32x16* o, int vb0, bf16x8 pa0, bf16x8 pa1, bf16x8 pa2, bf16x8 pa3) {
;     ...
;     A3_PAIR(o[0], o[1], A3_RDK(va, 2, 0), A3_RDK(va, 2, 1), A3_RDK(va, 2, 2), A3_RDK(va, 2, 3));
;     A3_PAIR(o[2], o[3], A3_RDK(vb, 0, 0), A3_RDK(vb, 0, 1), A3_RDK(vb, 0, 2), A3_RDK(vb, 0, 3));
;     A3_PAIR(o[4], o[5], A3_RDK(vb, 2, 0), A3_RDK(vb, 2, 1), A3_RDK(vb, 2, 2), A3_RDK(vb, 2, 3));
;     A3_PAIR(o[6], o[7], A3_NONE, A3_NONE, A3_NONE, A3_NONE);
; __device__ __forceinline__ void block(const Blk& B, char* lds, A3_LAS unsigned char* ldsl, const int tid) {
;     ...
;         asm volatile("s_waitcnt vmcnt(0)" ::: "memory");
;         __syncthreads();
	v_mfma_f32_32x32x16_bf16 v[82:97], v[138:141], v[156:159], v[82:97]
	v_mfma_f32_32x32x16_bf16 v[66:81], v[138:141], v[212:215], v[66:81]
	ds_read_b64_tr_b16 v[156:157], v160 offset:0x1000
	ds_read_b64_tr_b16 v[158:159], v160 offset:0x1800
	ds_read_b64_tr_b16 v[212:213], v160 offset:0x1200
	ds_read_b64_tr_b16 v[214:215], v160 offset:0x1a00
	s_waitcnt lgkmcnt(12)
	v_mfma_f32_32x32x16_bf16 v[82:97], v[134:137], v[216:219], v[82:97]
	v_mfma_f32_32x32x16_bf16 v[66:81], v[134:137], v[220:223], v[66:81]
	ds_read_b64_tr_b16 v[216:217], v160 offset:0x2000
	ds_read_b64_tr_b16 v[218:219], v160 offset:0x2800
	ds_read_b64_tr_b16 v[220:221], v160 offset:0x2200
	ds_read_b64_tr_b16 v[222:223], v160 offset:0x2a00
	s_waitcnt lgkmcnt(12)
	v_mfma_f32_32x32x16_bf16 v[82:97], v[130:133], v[224:227], v[82:97]
	v_mfma_f32_32x32x16_bf16 v[66:81], v[130:133], v[228:231], v[66:81]
	ds_read_b64_tr_b16 v[224:225], v160 offset:0x3000
	ds_read_b64_tr_b16 v[226:227], v160 offset:0x3800
	ds_read_b64_tr_b16 v[228:229], v160 offset:0x3200
	ds_read_b64_tr_b16 v[230:231], v160 offset:0x3a00
	s_waitcnt lgkmcnt(12)
	v_mfma_f32_32x32x16_bf16 v[50:65], v[142:145], v[148:151], v[50:65]
	v_mfma_f32_32x32x16_bf16 v[34:49], v[142:145], v[152:155], v[34:49]
	ds_read_b64_tr_b16 v[148:149], v160 offset:0x400
	ds_read_b64_tr_b16 v[150:151], v160 offset:0xc00
	ds_read_b64_tr_b16 v[152:153], v160 offset:0x600
	ds_read_b64_tr_b16 v[154:155], v160 offset:0xe00
	s_waitcnt lgkmcnt(12)
	v_mfma_f32_32x32x16_bf16 v[50:65], v[138:141], v[156:159], v[50:65]
	v_mfma_f32_32x32x16_bf16 v[34:49], v[138:141], v[212:215], v[34:49]
	ds_read_b64_tr_b16 v[156:157], v160 offset:0x1400
	ds_read_b64_tr_b16 v[158:159], v160 offset:0x1c00
	ds_read_b64_tr_b16 v[212:213], v160 offset:0x1600
	ds_read_b64_tr_b16 v[214:215], v160 offset:0x1e00
	s_waitcnt lgkmcnt(12)
	v_mfma_f32_32x32x16_bf16 v[50:65], v[134:137], v[216:219], v[50:65]
	v_mfma_f32_32x32x16_bf16 v[34:49], v[134:137], v[220:223], v[34:49]
	ds_read_b64_tr_b16 v[216:217], v160 offset:0x2400
	ds_read_b64_tr_b16 v[218:219], v160 offset:0x2c00
	ds_read_b64_tr_b16 v[220:221], v160 offset:0x2600
	ds_read_b64_tr_b16 v[222:223], v160 offset:0x2e00
	s_waitcnt lgkmcnt(12)
	v_mfma_f32_32x32x16_bf16 v[50:65], v[130:133], v[224:227], v[50:65]
	v_mfma_f32_32x32x16_bf16 v[34:49], v[130:133], v[228:231], v[34:49]
	ds_read_b64_tr_b16 v[224:225], v160 offset:0x3400
	ds_read_b64_tr_b16 v[226:227], v160 offset:0x3c00
	ds_read_b64_tr_b16 v[228:229], v160 offset:0x3600
	ds_read_b64_tr_b16 v[230:231], v160 offset:0x3e00
	s_waitcnt lgkmcnt(12)
	v_mfma_f32_32x32x16_bf16 v[18:33], v[142:145], v[148:151], v[18:33]
	v_mfma_f32_32x32x16_bf16 v[2:17], v[142:145], v[152:155], v[2:17]
	s_waitcnt lgkmcnt(0)
	s_waitcnt lgkmcnt(12)
	v_mfma_f32_32x32x16_bf16 v[18:33], v[138:141], v[156:159], v[18:33]
	v_mfma_f32_32x32x16_bf16 v[2:17], v[138:141], v[212:215], v[2:17]
	s_waitcnt lgkmcnt(0)
	s_waitcnt lgkmcnt(12)
	v_mfma_f32_32x32x16_bf16 v[18:33], v[134:137], v[216:219], v[18:33]
	v_mfma_f32_32x32x16_bf16 v[2:17], v[134:137], v[220:223], v[2:17]
	s_waitcnt lgkmcnt(0)
	s_waitcnt lgkmcnt(12)
	v_mfma_f32_32x32x16_bf16 v[18:33], v[130:133], v[224:227], v[18:33]
	v_mfma_f32_32x32x16_bf16 v[2:17], v[130:133], v[228:231], v[2:17]
	s_waitcnt lgkmcnt(0)
	s_cmp_lt_u32 s19, 0x2000
	s_cbranch_scc0 .Latt_wconv
	s_waitcnt vmcnt(0)
	s_branch .Latt_wd
.Latt_wconv:
	s_cmp_lt_u32 s5, 3
	s_cbranch_scc1 .Latt_w4
	s_cmp_lt_u32 s5, 4
	s_cbranch_scc1 .Latt_w6
	s_waitcnt vmcnt(8)
	s_branch .Latt_wd
.Latt_w6:
	s_waitcnt vmcnt(6)
	s_branch .Latt_wd

; __device__ __forceinline__ void block(const Blk& B, char* lds, A3_LAS unsigned char* ldsl, const int tid) {
;     ...
;     for (int t = 0; t < NT; ++t) {
;         const int buf = t & 1, kb = t * 64;
;         if (t + 1 < NT) A3_STAGE(t + 1, buf ^ 1);
;     ...
;         pv256(o, vb0 + buf * 32768, pa0, pa1, pa2, pa3);
;         asm volatile("s_waitcnt vmcnt(0)" ::: "memory");
;         __syncthreads();
;     }
.Latt_wd:
	s_add_i32 s63, s63, 0x4000
	s_cmp_eq_u32 s63, 0xc000
	s_cselect_b32 s63, 0, s63
	s_add_u32 s58, s58, 0x4000
	s_addc_u32 s59, s59, 0
	s_add_i32 s62, s62, 64
	s_add_i32 s5, s5, 1
	v_subrev_u32_e32 v211, 64, v211
	s_cmp_eq_u32 s17, s62
	s_barrier
	s_cbranch_scc1 .LBB0_338
	v_mov_b32_e32 v213, v0
	v_mov_b32_e32 v212, v146
	s_branch .LBB0_324

; __global__ void __launch_bounds__(NWAVES * 64, 2) mk_fwd(Args args) {
	.amdhsa_kernel _Z6mk_fwd4Args
		.amdhsa_group_segment_fixed_size 0
		.amdhsa_private_segment_fixed_size 0
		.amdhsa_kernarg_size 480
		.amdhsa_user_sgpr_count 2
		.amdhsa_user_sgpr_dispatch_ptr 0
		.amdhsa_user_sgpr_queue_ptr 0
		.amdhsa_user_sgpr_kernarg_segment_ptr 1
		.amdhsa_user_sgpr_dispatch_id 0
		.amdhsa_user_sgpr_kernarg_preload_length 0
		.amdhsa_user_sgpr_kernarg_preload_offset 0
		.amdhsa_user_sgpr_private_segment_size 0
		.amdhsa_uses_dynamic_stack 0
		.amdhsa_enable_private_segment 0
		.amdhsa_system_sgpr_workgroup_id_x 1
		.amdhsa_system_sgpr_workgroup_id_y 0
		.amdhsa_system_sgpr_workgroup_id_z 0
		.amdhsa_system_sgpr_workgroup_info 0
		.amdhsa_system_vgpr_workitem_id 0
		.amdhsa_next_free_vgpr 252
		.amdhsa_next_free_sgpr 102
		.amdhsa_accum_offset 252
		.amdhsa_reserve_vcc 1
		.amdhsa_float_round_mode_32 0
		.amdhsa_float_round_mode_16_64 0
		.amdhsa_float_denorm_mode_32 3
		.amdhsa_float_denorm_mode_16_64 3
		.amdhsa_dx10_clamp 1
		.amdhsa_ieee_mode 1
		.amdhsa_fp16_overflow 0
		.amdhsa_tg_split 0
		.amdhsa_exception_fp_ieee_invalid_op 0
		.amdhsa_exception_fp_denorm_src 0
		.amdhsa_exception_fp_ieee_div_zero 0
		.amdhsa_exception_fp_ieee_overflow 0
		.amdhsa_exception_fp_ieee_underflow 0
		.amdhsa_exception_fp_ieee_inexact 0
		.amdhsa_exception_int_div_zero 0
	.end_amdhsa_kernel

; __global__ void __launch_bounds__(NWAVES * 64, 2) mk_fwd(Args args) {
amdhsa.kernels:
  - .agpr_count:     0
    .args:
      - .offset:         0
        .size:           224
        .value_kind:     by_value
      - .offset:         224
        .size:           4
        .value_kind:     hidden_block_count_x
      - .offset:         228
        .size:           4
        .value_kind:     hidden_block_count_y
      - .offset:         232
        .size:           4
        .value_kind:     hidden_block_count_z
      - .offset:         236
        .size:           2
        .value_kind:     hidden_group_size_x
      - .offset:         238
        .size:           2
        .value_kind:     hidden_group_size_y
      - .offset:         240
        .size:           2
        .value_kind:     hidden_group_size_z
      - .offset:         242
        .size:           2
        .value_kind:     hidden_remainder_x
      - .offset:         244
        .size:           2
        .value_kind:     hidden_remainder_y
      - .offset:         246
        .size:           2
        .value_kind:     hidden_remainder_z
      - .offset:         264
        .size:           8
        .value_kind:     hidden_global_offset_x
      - .offset:         272
        .size:           8
        .value_kind:     hidden_global_offset_y
      - .offset:         280
        .size:           8
        .value_kind:     hidden_global_offset_z
      - .offset:         288
        .size:           2
        .value_kind:     hidden_grid_dims
      - .offset:         344
        .size:           4
        .value_kind:     hidden_dynamic_lds_size
    .group_segment_fixed_size: 0
    .kernarg_segment_align: 8
    .kernarg_segment_size: 480
    .language:       OpenCL C
    .language_version:
      - 2
      - 0
    .max_flat_workgroup_size: 512
    .name:           _Z6mk_fwd4Args
    .private_segment_fixed_size: 0
    .sgpr_count:     108
    .sgpr_spill_count: 11
    .symbol:         _Z6mk_fwd4Args.kd
    .uniform_work_group_size: 1
    .uses_dynamic_stack: false
    .vgpr_count:     252
    .vgpr_spill_count: 0
    .wavefront_size: 64
